# expert-up SwiGLU epilogue regenerated with packed f32 ops (v_pk_add/v_pk_mul on adjacent accumulator pairs, in place), same math order
# speedup vs baseline: 1.0053x; 1.0032x over previous
.LBB0_1094:
	v_mov_b32_e32 v18, v188
	s_nop 15
	s_nop 15
	s_lshl_b32 s31, s36, 7
	v_readfirstlane_b32 s30, v18
	s_lshr_b32 s36, s30, 1
	s_and_b32 s36, s36, 0x60
	s_or_b32 s31, s36, s31
	v_lshrrev_b32_e32 v0, 1, v18
	v_ashrrev_i32_e32 v167, 31, v166
	v_and_or_b32 v16, v0, 24, s31
	v_lshlrev_b64 v[0:1], 13, v[166:167]
	v_lshl_add_u64 v[0:1], s[28:29], 0, v[0:1]
	v_ashrrev_i32_e32 v17, 31, v16
	v_lshl_add_u64 v[8:9], v[16:17], 2, v[0:1]
	global_load_dwordx4 v[0:3], v[8:9], off offset:16
	global_load_dwordx4 v[4:7], v[8:9], off
	s_movk_i32 s31, 0x1000
	v_lshl_add_u64 v[10:11], v[8:9], 0, s[84:85]
	v_add_co_u32_e32 v8, vcc, s31, v8
	s_ashr_i32 s30, s30, 2
	s_nop 0
	v_addc_co_u32_e32 v9, vcc, 0, v9, vcc
	global_load_dwordx4 v[12:15], v[8:9], off
	s_nop 0
	global_load_dwordx4 v[8:11], v[10:11], off offset:16
	v_lshlrev_b32_e32 v19, 8, v219
	s_andn2_b32 s30, s30, 63
	v_add_u32_e32 v19, s30, v19
	v_and_or_b32 v18, v18, 15, v19
	v_ashrrev_i32_e32 v19, 31, v18
	v_readlane_b32 s30, v254, 30
	v_lshlrev_b64 v[18:19], 10, v[18:19]
	v_readlane_b32 s31, v254, 31
	s_mov_b32 s21, 0x24000
	s_mov_b64 s[40:41], -1
	v_lshl_add_u64 v[18:19], s[30:31], 0, v[18:19]
	v_lshl_add_u64 v[16:17], v[18:19], 0, v[16:17]
	s_mov_b32 s30, 0xc000
	s_mov_b64 s[72:73], 0x400
	v_readlane_b32 s70, v255, 14
	s_mov_b32 s71, s66
	s_waitcnt vmcnt(0)
	s_mov_b32 s98, 0xc01d265f
	v_pk_add_f32 v[8:9], v[8:9], 1.0 op_sel_hi:[1,0]
	v_pk_add_f32 v[10:11], v[10:11], 1.0 op_sel_hi:[1,0]
	v_pk_add_f32 v[12:13], v[12:13], 1.0 op_sel_hi:[1,0]
	v_pk_add_f32 v[14:15], v[14:15], 1.0 op_sel_hi:[1,0]
	v_pk_add_f32 v[158:159], v[158:159], v[4:5]
	v_pk_add_f32 v[160:161], v[160:161], v[6:7]
	v_pk_add_f32 v[150:151], v[150:151], v[0:1]
	v_pk_add_f32 v[152:153], v[152:153], v[2:3]
	v_min_f32_e32 v158, 0x40e00000, v158
	v_min_f32_e32 v159, 0x40e00000, v159
	v_min_f32_e32 v160, 0x40e00000, v160
	v_min_f32_e32 v161, 0x40e00000, v161
	v_min_f32_e32 v150, 0x40e00000, v150
	v_min_f32_e32 v151, 0x40e00000, v151
	v_min_f32_e32 v152, 0x40e00000, v152
	v_min_f32_e32 v153, 0x40e00000, v153
	v_pk_mul_f32 v[18:19], v[158:159], s[98:99] op_sel_hi:[1,0]
	v_pk_mul_f32 v[20:21], v[160:161], s[98:99] op_sel_hi:[1,0]
	v_pk_mul_f32 v[22:23], v[150:151], s[98:99] op_sel_hi:[1,0]
	v_pk_mul_f32 v[24:25], v[152:153], s[98:99] op_sel_hi:[1,0]
	v_exp_f32_e32 v18, v18
	v_exp_f32_e32 v19, v19
	v_exp_f32_e32 v20, v20
	v_exp_f32_e32 v21, v21
	v_exp_f32_e32 v22, v22
	v_exp_f32_e32 v23, v23
	v_exp_f32_e32 v24, v24
	v_exp_f32_e32 v25, v25
	v_pk_add_f32 v[154:155], v[154:155], v[12:13]
	v_pk_add_f32 v[156:157], v[156:157], v[14:15]
	v_pk_add_f32 v[146:147], v[146:147], v[8:9]
	v_pk_add_f32 v[148:149], v[148:149], v[10:11]
	v_pk_add_f32 v[18:19], v[18:19], 1.0 op_sel_hi:[1,0]
	v_pk_add_f32 v[20:21], v[20:21], 1.0 op_sel_hi:[1,0]
	v_pk_add_f32 v[22:23], v[22:23], 1.0 op_sel_hi:[1,0]
	v_pk_add_f32 v[24:25], v[24:25], 1.0 op_sel_hi:[1,0]
	v_rcp_f32_e32 v18, v18
	v_rcp_f32_e32 v19, v19
	v_rcp_f32_e32 v20, v20
	v_rcp_f32_e32 v21, v21
	v_rcp_f32_e32 v22, v22
	v_rcp_f32_e32 v23, v23
	v_rcp_f32_e32 v24, v24
	v_rcp_f32_e32 v25, v25
	v_med3_f32 v154, v154, s61, v214
	v_med3_f32 v155, v155, s61, v214
	v_med3_f32 v156, v156, s61, v214
	v_med3_f32 v157, v157, s61, v214
	v_med3_f32 v146, v146, s61, v214
	v_med3_f32 v147, v147, s61, v214
	v_med3_f32 v148, v148, s61, v214
	v_med3_f32 v149, v149, s61, v214
	v_pk_mul_f32 v[158:159], v[158:159], v[18:19]
	v_pk_mul_f32 v[160:161], v[160:161], v[20:21]
	v_pk_mul_f32 v[150:151], v[150:151], v[22:23]
	v_pk_mul_f32 v[152:153], v[152:153], v[24:25]
	v_pk_mul_f32 v[158:159], v[154:155], v[158:159]
	v_pk_mul_f32 v[160:161], v[156:157], v[160:161]
	v_pk_mul_f32 v[150:151], v[146:147], v[150:151]
	v_pk_mul_f32 v[152:153], v[148:149], v[152:153]
	v_cvt_pk_fp8_f32 v26, v158, v159
	v_cvt_pk_fp8_f32 v26, v160, v161 op_sel:[0,0,1]
	v_cvt_pk_fp8_f32 v27, v150, v151
	v_cvt_pk_fp8_f32 v27, v152, v153 op_sel:[0,0,1]
	global_store_dwordx2 v[16:17], v[26:27], off
	v_add_co_u32_e32 v154, vcc, s62, v16
	v_addc_co_u32_e32 v155, vcc, 0, v17, vcc
	v_pk_add_f32 v[142:143], v[142:143], v[4:5]
	v_pk_add_f32 v[144:145], v[144:145], v[6:7]
	v_pk_add_f32 v[134:135], v[134:135], v[0:1]
	v_pk_add_f32 v[136:137], v[136:137], v[2:3]
	v_min_f32_e32 v142, 0x40e00000, v142
	v_min_f32_e32 v143, 0x40e00000, v143
	v_min_f32_e32 v144, 0x40e00000, v144
	v_min_f32_e32 v145, 0x40e00000, v145
	v_min_f32_e32 v134, 0x40e00000, v134
	v_min_f32_e32 v135, 0x40e00000, v135
	v_min_f32_e32 v136, 0x40e00000, v136
	v_min_f32_e32 v137, 0x40e00000, v137
	v_pk_mul_f32 v[18:19], v[142:143], s[98:99] op_sel_hi:[1,0]
	v_pk_mul_f32 v[20:21], v[144:145], s[98:99] op_sel_hi:[1,0]
	v_pk_mul_f32 v[22:23], v[134:135], s[98:99] op_sel_hi:[1,0]
	v_pk_mul_f32 v[24:25], v[136:137], s[98:99] op_sel_hi:[1,0]
	v_exp_f32_e32 v18, v18
	v_exp_f32_e32 v19, v19
	v_exp_f32_e32 v20, v20
	v_exp_f32_e32 v21, v21
	v_exp_f32_e32 v22, v22
	v_exp_f32_e32 v23, v23
	v_exp_f32_e32 v24, v24
	v_exp_f32_e32 v25, v25
	v_pk_add_f32 v[138:139], v[138:139], v[12:13]
	v_pk_add_f32 v[140:141], v[140:141], v[14:15]
	v_pk_add_f32 v[130:131], v[130:131], v[8:9]
	v_pk_add_f32 v[132:133], v[132:133], v[10:11]
	v_pk_add_f32 v[18:19], v[18:19], 1.0 op_sel_hi:[1,0]
	v_pk_add_f32 v[20:21], v[20:21], 1.0 op_sel_hi:[1,0]
	v_pk_add_f32 v[22:23], v[22:23], 1.0 op_sel_hi:[1,0]
	v_pk_add_f32 v[24:25], v[24:25], 1.0 op_sel_hi:[1,0]
	v_rcp_f32_e32 v18, v18
	v_rcp_f32_e32 v19, v19
	v_rcp_f32_e32 v20, v20
	v_rcp_f32_e32 v21, v21
	v_rcp_f32_e32 v22, v22
	v_rcp_f32_e32 v23, v23
	v_rcp_f32_e32 v24, v24
	v_rcp_f32_e32 v25, v25
	v_med3_f32 v138, v138, s61, v214
	v_med3_f32 v139, v139, s61, v214
	v_med3_f32 v140, v140, s61, v214
	v_med3_f32 v141, v141, s61, v214
	v_med3_f32 v130, v130, s61, v214
	v_med3_f32 v131, v131, s61, v214
	v_med3_f32 v132, v132, s61, v214
	v_med3_f32 v133, v133, s61, v214
	v_pk_mul_f32 v[142:143], v[142:143], v[18:19]
	v_pk_mul_f32 v[144:145], v[144:145], v[20:21]
	v_pk_mul_f32 v[134:135], v[134:135], v[22:23]
	v_pk_mul_f32 v[136:137], v[136:137], v[24:25]
	v_pk_mul_f32 v[142:143], v[138:139], v[142:143]
	v_pk_mul_f32 v[144:145], v[140:141], v[144:145]
	v_pk_mul_f32 v[134:135], v[130:131], v[134:135]
	v_pk_mul_f32 v[136:137], v[132:133], v[136:137]
	v_cvt_pk_fp8_f32 v26, v142, v143
	v_cvt_pk_fp8_f32 v26, v144, v145 op_sel:[0,0,1]
	v_cvt_pk_fp8_f32 v27, v134, v135
	v_cvt_pk_fp8_f32 v27, v136, v137 op_sel:[0,0,1]
	global_store_dwordx2 v[154:155], v[26:27], off
	v_add_co_u32_e32 v154, vcc, s24, v16
	v_addc_co_u32_e32 v155, vcc, 0, v17, vcc
	v_pk_add_f32 v[126:127], v[126:127], v[4:5]
	v_pk_add_f32 v[128:129], v[128:129], v[6:7]
	v_pk_add_f32 v[118:119], v[118:119], v[0:1]
	v_pk_add_f32 v[120:121], v[120:121], v[2:3]
	v_min_f32_e32 v126, 0x40e00000, v126
	v_min_f32_e32 v127, 0x40e00000, v127
	v_min_f32_e32 v128, 0x40e00000, v128
	v_min_f32_e32 v129, 0x40e00000, v129
	v_min_f32_e32 v118, 0x40e00000, v118
	v_min_f32_e32 v119, 0x40e00000, v119
	v_min_f32_e32 v120, 0x40e00000, v120
	v_min_f32_e32 v121, 0x40e00000, v121
	v_pk_mul_f32 v[18:19], v[126:127], s[98:99] op_sel_hi:[1,0]
	v_pk_mul_f32 v[20:21], v[128:129], s[98:99] op_sel_hi:[1,0]
	v_pk_mul_f32 v[22:23], v[118:119], s[98:99] op_sel_hi:[1,0]
	v_pk_mul_f32 v[24:25], v[120:121], s[98:99] op_sel_hi:[1,0]
	v_exp_f32_e32 v18, v18
	v_exp_f32_e32 v19, v19
	v_exp_f32_e32 v20, v20
	v_exp_f32_e32 v21, v21
	v_exp_f32_e32 v22, v22
	v_exp_f32_e32 v23, v23
	v_exp_f32_e32 v24, v24
	v_exp_f32_e32 v25, v25
	v_pk_add_f32 v[122:123], v[122:123], v[12:13]
	v_pk_add_f32 v[124:125], v[124:125], v[14:15]
	v_pk_add_f32 v[114:115], v[114:115], v[8:9]
	v_pk_add_f32 v[116:117], v[116:117], v[10:11]
	v_pk_add_f32 v[18:19], v[18:19], 1.0 op_sel_hi:[1,0]
	v_pk_add_f32 v[20:21], v[20:21], 1.0 op_sel_hi:[1,0]
	v_pk_add_f32 v[22:23], v[22:23], 1.0 op_sel_hi:[1,0]
	v_pk_add_f32 v[24:25], v[24:25], 1.0 op_sel_hi:[1,0]
	v_rcp_f32_e32 v18, v18
	v_rcp_f32_e32 v19, v19
	v_rcp_f32_e32 v20, v20
	v_rcp_f32_e32 v21, v21
	v_rcp_f32_e32 v22, v22
	v_rcp_f32_e32 v23, v23
	v_rcp_f32_e32 v24, v24
	v_rcp_f32_e32 v25, v25
	v_med3_f32 v122, v122, s61, v214
	v_med3_f32 v123, v123, s61, v214
	v_med3_f32 v124, v124, s61, v214
	v_med3_f32 v125, v125, s61, v214
	v_med3_f32 v114, v114, s61, v214
	v_med3_f32 v115, v115, s61, v214
	v_med3_f32 v116, v116, s61, v214
	v_med3_f32 v117, v117, s61, v214
	v_pk_mul_f32 v[126:127], v[126:127], v[18:19]
	v_pk_mul_f32 v[128:129], v[128:129], v[20:21]
	v_pk_mul_f32 v[118:119], v[118:119], v[22:23]
	v_pk_mul_f32 v[120:121], v[120:121], v[24:25]
	v_pk_mul_f32 v[126:127], v[122:123], v[126:127]
	v_pk_mul_f32 v[128:129], v[124:125], v[128:129]
	v_pk_mul_f32 v[118:119], v[114:115], v[118:119]
	v_pk_mul_f32 v[120:121], v[116:117], v[120:121]
	v_cvt_pk_fp8_f32 v26, v126, v127
	v_cvt_pk_fp8_f32 v26, v128, v129 op_sel:[0,0,1]
	v_cvt_pk_fp8_f32 v27, v118, v119
	v_cvt_pk_fp8_f32 v27, v120, v121 op_sel:[0,0,1]
	global_store_dwordx2 v[154:155], v[26:27], off
	v_add_co_u32_e32 v154, vcc, s30, v16
	v_addc_co_u32_e32 v155, vcc, 0, v17, vcc
	v_pk_add_f32 v[108:109], v[108:109], v[4:5]
	v_pk_add_f32 v[110:111], v[110:111], v[6:7]
	v_pk_add_f32 v[100:101], v[100:101], v[0:1]
	v_pk_add_f32 v[102:103], v[102:103], v[2:3]
	v_min_f32_e32 v108, 0x40e00000, v108
	v_min_f32_e32 v109, 0x40e00000, v109
	v_min_f32_e32 v110, 0x40e00000, v110
	v_min_f32_e32 v111, 0x40e00000, v111
	v_min_f32_e32 v100, 0x40e00000, v100
	v_min_f32_e32 v101, 0x40e00000, v101
	v_min_f32_e32 v102, 0x40e00000, v102
	v_min_f32_e32 v103, 0x40e00000, v103
	v_pk_mul_f32 v[18:19], v[108:109], s[98:99] op_sel_hi:[1,0]
	v_pk_mul_f32 v[20:21], v[110:111], s[98:99] op_sel_hi:[1,0]
	v_pk_mul_f32 v[22:23], v[100:101], s[98:99] op_sel_hi:[1,0]
	v_pk_mul_f32 v[24:25], v[102:103], s[98:99] op_sel_hi:[1,0]
	v_exp_f32_e32 v18, v18
	v_exp_f32_e32 v19, v19
	v_exp_f32_e32 v20, v20
	v_exp_f32_e32 v21, v21
	v_exp_f32_e32 v22, v22
	v_exp_f32_e32 v23, v23
	v_exp_f32_e32 v24, v24
	v_exp_f32_e32 v25, v25
	v_pk_add_f32 v[104:105], v[104:105], v[12:13]
	v_pk_add_f32 v[106:107], v[106:107], v[14:15]
	v_pk_add_f32 v[96:97], v[96:97], v[8:9]
	v_pk_add_f32 v[98:99], v[98:99], v[10:11]
	v_pk_add_f32 v[18:19], v[18:19], 1.0 op_sel_hi:[1,0]
	v_pk_add_f32 v[20:21], v[20:21], 1.0 op_sel_hi:[1,0]
	v_pk_add_f32 v[22:23], v[22:23], 1.0 op_sel_hi:[1,0]
	v_pk_add_f32 v[24:25], v[24:25], 1.0 op_sel_hi:[1,0]
	v_rcp_f32_e32 v18, v18
	v_rcp_f32_e32 v19, v19
	v_rcp_f32_e32 v20, v20
	v_rcp_f32_e32 v21, v21
	v_rcp_f32_e32 v22, v22
	v_rcp_f32_e32 v23, v23
	v_rcp_f32_e32 v24, v24
	v_rcp_f32_e32 v25, v25
	v_med3_f32 v104, v104, s61, v214
	v_med3_f32 v105, v105, s61, v214
	v_med3_f32 v106, v106, s61, v214
	v_med3_f32 v107, v107, s61, v214
	v_med3_f32 v96, v96, s61, v214
	v_med3_f32 v97, v97, s61, v214
	v_med3_f32 v98, v98, s61, v214
	v_med3_f32 v99, v99, s61, v214
	v_pk_mul_f32 v[108:109], v[108:109], v[18:19]
	v_pk_mul_f32 v[110:111], v[110:111], v[20:21]
	v_pk_mul_f32 v[100:101], v[100:101], v[22:23]
	v_pk_mul_f32 v[102:103], v[102:103], v[24:25]
	v_pk_mul_f32 v[108:109], v[104:105], v[108:109]
	v_pk_mul_f32 v[110:111], v[106:107], v[110:111]
	v_pk_mul_f32 v[100:101], v[96:97], v[100:101]
	v_pk_mul_f32 v[102:103], v[98:99], v[102:103]
	v_cvt_pk_fp8_f32 v26, v108, v109
	v_cvt_pk_fp8_f32 v26, v110, v111 op_sel:[0,0,1]
	v_cvt_pk_fp8_f32 v27, v100, v101
	v_cvt_pk_fp8_f32 v27, v102, v103 op_sel:[0,0,1]
	global_store_dwordx2 v[154:155], v[26:27], off
	v_add_co_u32_e32 v154, vcc, s63, v16
	v_addc_co_u32_e32 v155, vcc, 0, v17, vcc
	v_pk_add_f32 v[92:93], v[92:93], v[4:5]
	v_pk_add_f32 v[94:95], v[94:95], v[6:7]
	v_pk_add_f32 v[84:85], v[84:85], v[0:1]
	v_pk_add_f32 v[86:87], v[86:87], v[2:3]
	v_min_f32_e32 v92, 0x40e00000, v92
	v_min_f32_e32 v93, 0x40e00000, v93
	v_min_f32_e32 v94, 0x40e00000, v94
	v_min_f32_e32 v95, 0x40e00000, v95
	v_min_f32_e32 v84, 0x40e00000, v84
	v_min_f32_e32 v85, 0x40e00000, v85
	v_min_f32_e32 v86, 0x40e00000, v86
	v_min_f32_e32 v87, 0x40e00000, v87
	v_pk_mul_f32 v[18:19], v[92:93], s[98:99] op_sel_hi:[1,0]
	v_pk_mul_f32 v[20:21], v[94:95], s[98:99] op_sel_hi:[1,0]
	v_pk_mul_f32 v[22:23], v[84:85], s[98:99] op_sel_hi:[1,0]
	v_pk_mul_f32 v[24:25], v[86:87], s[98:99] op_sel_hi:[1,0]
	v_exp_f32_e32 v18, v18
	v_exp_f32_e32 v19, v19
	v_exp_f32_e32 v20, v20
	v_exp_f32_e32 v21, v21
	v_exp_f32_e32 v22, v22
	v_exp_f32_e32 v23, v23
	v_exp_f32_e32 v24, v24
	v_exp_f32_e32 v25, v25
	v_pk_add_f32 v[88:89], v[88:89], v[12:13]
	v_pk_add_f32 v[90:91], v[90:91], v[14:15]
	v_pk_add_f32 v[80:81], v[80:81], v[8:9]
	v_pk_add_f32 v[82:83], v[82:83], v[10:11]
	v_pk_add_f32 v[18:19], v[18:19], 1.0 op_sel_hi:[1,0]
	v_pk_add_f32 v[20:21], v[20:21], 1.0 op_sel_hi:[1,0]
	v_pk_add_f32 v[22:23], v[22:23], 1.0 op_sel_hi:[1,0]
	v_pk_add_f32 v[24:25], v[24:25], 1.0 op_sel_hi:[1,0]
	v_rcp_f32_e32 v18, v18
	v_rcp_f32_e32 v19, v19
	v_rcp_f32_e32 v20, v20
	v_rcp_f32_e32 v21, v21
	v_rcp_f32_e32 v22, v22
	v_rcp_f32_e32 v23, v23
	v_rcp_f32_e32 v24, v24
	v_rcp_f32_e32 v25, v25
	v_med3_f32 v88, v88, s61, v214
	v_med3_f32 v89, v89, s61, v214
	v_med3_f32 v90, v90, s61, v214
	v_med3_f32 v91, v91, s61, v214
	v_med3_f32 v80, v80, s61, v214
	v_med3_f32 v81, v81, s61, v214
	v_med3_f32 v82, v82, s61, v214
	v_med3_f32 v83, v83, s61, v214
	v_pk_mul_f32 v[92:93], v[92:93], v[18:19]
	v_pk_mul_f32 v[94:95], v[94:95], v[20:21]
	v_pk_mul_f32 v[84:85], v[84:85], v[22:23]
	v_pk_mul_f32 v[86:87], v[86:87], v[24:25]
	v_pk_mul_f32 v[92:93], v[88:89], v[92:93]
	v_pk_mul_f32 v[94:95], v[90:91], v[94:95]
	v_pk_mul_f32 v[84:85], v[80:81], v[84:85]
	v_pk_mul_f32 v[86:87], v[82:83], v[86:87]
	v_cvt_pk_fp8_f32 v26, v92, v93
	v_cvt_pk_fp8_f32 v26, v94, v95 op_sel:[0,0,1]
	v_cvt_pk_fp8_f32 v27, v84, v85
	v_cvt_pk_fp8_f32 v27, v86, v87 op_sel:[0,0,1]
	global_store_dwordx2 v[154:155], v[26:27], off
	v_add_co_u32_e32 v154, vcc, s21, v16
	v_addc_co_u32_e32 v155, vcc, 0, v17, vcc
	s_mov_b32 s21, 0x28000
	v_pk_add_f32 v[76:77], v[76:77], v[4:5]
	v_pk_add_f32 v[78:79], v[78:79], v[6:7]
	v_pk_add_f32 v[68:69], v[68:69], v[0:1]
	v_pk_add_f32 v[70:71], v[70:71], v[2:3]
	v_min_f32_e32 v76, 0x40e00000, v76
	v_min_f32_e32 v77, 0x40e00000, v77
	v_min_f32_e32 v78, 0x40e00000, v78
	v_min_f32_e32 v79, 0x40e00000, v79
	v_min_f32_e32 v68, 0x40e00000, v68
	v_min_f32_e32 v69, 0x40e00000, v69
	v_min_f32_e32 v70, 0x40e00000, v70
	v_min_f32_e32 v71, 0x40e00000, v71
	v_pk_mul_f32 v[18:19], v[76:77], s[98:99] op_sel_hi:[1,0]
	v_pk_mul_f32 v[20:21], v[78:79], s[98:99] op_sel_hi:[1,0]
	v_pk_mul_f32 v[22:23], v[68:69], s[98:99] op_sel_hi:[1,0]
	v_pk_mul_f32 v[24:25], v[70:71], s[98:99] op_sel_hi:[1,0]
	v_exp_f32_e32 v18, v18
	v_exp_f32_e32 v19, v19
	v_exp_f32_e32 v20, v20
	v_exp_f32_e32 v21, v21
	v_exp_f32_e32 v22, v22
	v_exp_f32_e32 v23, v23
	v_exp_f32_e32 v24, v24
	v_exp_f32_e32 v25, v25
	v_pk_add_f32 v[72:73], v[72:73], v[12:13]
	v_pk_add_f32 v[74:75], v[74:75], v[14:15]
	v_pk_add_f32 v[64:65], v[64:65], v[8:9]
	v_pk_add_f32 v[66:67], v[66:67], v[10:11]
	v_pk_add_f32 v[18:19], v[18:19], 1.0 op_sel_hi:[1,0]
	v_pk_add_f32 v[20:21], v[20:21], 1.0 op_sel_hi:[1,0]
	v_pk_add_f32 v[22:23], v[22:23], 1.0 op_sel_hi:[1,0]
	v_pk_add_f32 v[24:25], v[24:25], 1.0 op_sel_hi:[1,0]
	v_rcp_f32_e32 v18, v18
	v_rcp_f32_e32 v19, v19
	v_rcp_f32_e32 v20, v20
	v_rcp_f32_e32 v21, v21
	v_rcp_f32_e32 v22, v22
	v_rcp_f32_e32 v23, v23
	v_rcp_f32_e32 v24, v24
	v_rcp_f32_e32 v25, v25
	v_med3_f32 v72, v72, s61, v214
	v_med3_f32 v73, v73, s61, v214
	v_med3_f32 v74, v74, s61, v214
	v_med3_f32 v75, v75, s61, v214
	v_med3_f32 v64, v64, s61, v214
	v_med3_f32 v65, v65, s61, v214
	v_med3_f32 v66, v66, s61, v214
	v_med3_f32 v67, v67, s61, v214
	v_pk_mul_f32 v[76:77], v[76:77], v[18:19]
	v_pk_mul_f32 v[78:79], v[78:79], v[20:21]
	v_pk_mul_f32 v[68:69], v[68:69], v[22:23]
	v_pk_mul_f32 v[70:71], v[70:71], v[24:25]
	v_pk_mul_f32 v[76:77], v[72:73], v[76:77]
	v_pk_mul_f32 v[78:79], v[74:75], v[78:79]
	v_pk_mul_f32 v[68:69], v[64:65], v[68:69]
	v_pk_mul_f32 v[70:71], v[66:67], v[70:71]
	v_cvt_pk_fp8_f32 v26, v76, v77
	v_cvt_pk_fp8_f32 v26, v78, v79 op_sel:[0,0,1]
	v_cvt_pk_fp8_f32 v27, v68, v69
	v_cvt_pk_fp8_f32 v27, v70, v71 op_sel:[0,0,1]
	global_store_dwordx2 v[154:155], v[26:27], off
	v_add_co_u32_e32 v154, vcc, s21, v16
	v_addc_co_u32_e32 v155, vcc, 0, v17, vcc
	s_mov_b32 s21, s20
	v_pk_add_f32 v[60:61], v[60:61], v[4:5]
	v_pk_add_f32 v[62:63], v[62:63], v[6:7]
	v_pk_add_f32 v[52:53], v[52:53], v[0:1]
	v_pk_add_f32 v[54:55], v[54:55], v[2:3]
	v_min_f32_e32 v60, 0x40e00000, v60
	v_min_f32_e32 v61, 0x40e00000, v61
	v_min_f32_e32 v62, 0x40e00000, v62
	v_min_f32_e32 v63, 0x40e00000, v63
	v_min_f32_e32 v52, 0x40e00000, v52
	v_min_f32_e32 v53, 0x40e00000, v53
	v_min_f32_e32 v54, 0x40e00000, v54
	v_min_f32_e32 v55, 0x40e00000, v55
	v_pk_mul_f32 v[18:19], v[60:61], s[98:99] op_sel_hi:[1,0]
	v_pk_mul_f32 v[20:21], v[62:63], s[98:99] op_sel_hi:[1,0]
	v_pk_mul_f32 v[22:23], v[52:53], s[98:99] op_sel_hi:[1,0]
	v_pk_mul_f32 v[24:25], v[54:55], s[98:99] op_sel_hi:[1,0]
	v_exp_f32_e32 v18, v18
	v_exp_f32_e32 v19, v19
	v_exp_f32_e32 v20, v20
	v_exp_f32_e32 v21, v21
	v_exp_f32_e32 v22, v22
	v_exp_f32_e32 v23, v23
	v_exp_f32_e32 v24, v24
	v_exp_f32_e32 v25, v25
	v_pk_add_f32 v[56:57], v[56:57], v[12:13]
	v_pk_add_f32 v[58:59], v[58:59], v[14:15]
	v_pk_add_f32 v[48:49], v[48:49], v[8:9]
	v_pk_add_f32 v[50:51], v[50:51], v[10:11]
	v_pk_add_f32 v[18:19], v[18:19], 1.0 op_sel_hi:[1,0]
	v_pk_add_f32 v[20:21], v[20:21], 1.0 op_sel_hi:[1,0]
	v_pk_add_f32 v[22:23], v[22:23], 1.0 op_sel_hi:[1,0]
	v_pk_add_f32 v[24:25], v[24:25], 1.0 op_sel_hi:[1,0]
	v_rcp_f32_e32 v18, v18
	v_rcp_f32_e32 v19, v19
	v_rcp_f32_e32 v20, v20
	v_rcp_f32_e32 v21, v21
	v_rcp_f32_e32 v22, v22
	v_rcp_f32_e32 v23, v23
	v_rcp_f32_e32 v24, v24
	v_rcp_f32_e32 v25, v25
	v_med3_f32 v56, v56, s61, v214
	v_med3_f32 v57, v57, s61, v214
	v_med3_f32 v58, v58, s61, v214
	v_med3_f32 v59, v59, s61, v214
	v_med3_f32 v48, v48, s61, v214
	v_med3_f32 v49, v49, s61, v214
	v_med3_f32 v50, v50, s61, v214
	v_med3_f32 v51, v51, s61, v214
	v_pk_mul_f32 v[60:61], v[60:61], v[18:19]
	v_pk_mul_f32 v[62:63], v[62:63], v[20:21]
	v_pk_mul_f32 v[52:53], v[52:53], v[22:23]
	v_pk_mul_f32 v[54:55], v[54:55], v[24:25]
	v_pk_mul_f32 v[60:61], v[56:57], v[60:61]
	v_pk_mul_f32 v[62:63], v[58:59], v[62:63]
	v_pk_mul_f32 v[52:53], v[48:49], v[52:53]
	v_pk_mul_f32 v[54:55], v[50:51], v[54:55]
	v_cvt_pk_fp8_f32 v26, v60, v61
	v_cvt_pk_fp8_f32 v26, v62, v63 op_sel:[0,0,1]
	v_cvt_pk_fp8_f32 v27, v52, v53
	v_cvt_pk_fp8_f32 v27, v54, v55 op_sel:[0,0,1]
	global_store_dwordx2 v[154:155], v[26:27], off
	v_add_co_u32_e32 v154, vcc, 0x2c000, v16
	v_addc_co_u32_e32 v155, vcc, 0, v17, vcc
	s_and_b64 vcc, exec, s[38:39]
	v_pk_add_f32 v[44:45], v[44:45], v[4:5]
	v_pk_add_f32 v[46:47], v[46:47], v[6:7]
	v_pk_add_f32 v[36:37], v[36:37], v[0:1]
	v_pk_add_f32 v[38:39], v[38:39], v[2:3]
	v_min_f32_e32 v44, 0x40e00000, v44
	v_min_f32_e32 v45, 0x40e00000, v45
	v_min_f32_e32 v46, 0x40e00000, v46
	v_min_f32_e32 v47, 0x40e00000, v47
	v_min_f32_e32 v36, 0x40e00000, v36
	v_min_f32_e32 v37, 0x40e00000, v37
	v_min_f32_e32 v38, 0x40e00000, v38
	v_min_f32_e32 v39, 0x40e00000, v39
	v_pk_mul_f32 v[18:19], v[44:45], s[98:99] op_sel_hi:[1,0]
	v_pk_mul_f32 v[20:21], v[46:47], s[98:99] op_sel_hi:[1,0]
	v_pk_mul_f32 v[22:23], v[36:37], s[98:99] op_sel_hi:[1,0]
	v_pk_mul_f32 v[24:25], v[38:39], s[98:99] op_sel_hi:[1,0]
	v_exp_f32_e32 v18, v18
	v_exp_f32_e32 v19, v19
	v_exp_f32_e32 v20, v20
	v_exp_f32_e32 v21, v21
	v_exp_f32_e32 v22, v22
	v_exp_f32_e32 v23, v23
	v_exp_f32_e32 v24, v24
	v_exp_f32_e32 v25, v25
	v_pk_add_f32 v[40:41], v[40:41], v[12:13]
	v_pk_add_f32 v[42:43], v[42:43], v[14:15]
	v_pk_add_f32 v[32:33], v[32:33], v[8:9]
	v_pk_add_f32 v[34:35], v[34:35], v[10:11]
	v_pk_add_f32 v[18:19], v[18:19], 1.0 op_sel_hi:[1,0]
	v_pk_add_f32 v[20:21], v[20:21], 1.0 op_sel_hi:[1,0]
	v_pk_add_f32 v[22:23], v[22:23], 1.0 op_sel_hi:[1,0]
	v_pk_add_f32 v[24:25], v[24:25], 1.0 op_sel_hi:[1,0]
	v_rcp_f32_e32 v18, v18
	v_rcp_f32_e32 v19, v19
	v_rcp_f32_e32 v20, v20
	v_rcp_f32_e32 v21, v21
	v_rcp_f32_e32 v22, v22
	v_rcp_f32_e32 v23, v23
	v_rcp_f32_e32 v24, v24
	v_rcp_f32_e32 v25, v25
	v_med3_f32 v40, v40, s61, v214
	v_med3_f32 v41, v41, s61, v214
	v_med3_f32 v42, v42, s61, v214
	v_med3_f32 v43, v43, s61, v214
	v_med3_f32 v32, v32, s61, v214
	v_med3_f32 v33, v33, s61, v214
	v_med3_f32 v34, v34, s61, v214
	v_med3_f32 v35, v35, s61, v214
	v_pk_mul_f32 v[44:45], v[44:45], v[18:19]
	v_pk_mul_f32 v[46:47], v[46:47], v[20:21]
	v_pk_mul_f32 v[36:37], v[36:37], v[22:23]
	v_pk_mul_f32 v[38:39], v[38:39], v[24:25]
	v_pk_mul_f32 v[44:45], v[40:41], v[44:45]
	v_pk_mul_f32 v[46:47], v[42:43], v[46:47]
	v_pk_mul_f32 v[36:37], v[32:33], v[36:37]
	v_pk_mul_f32 v[38:39], v[34:35], v[38:39]
	v_cvt_pk_fp8_f32 v26, v44, v45
	v_cvt_pk_fp8_f32 v26, v46, v47 op_sel:[0,0,1]
	v_cvt_pk_fp8_f32 v27, v36, v37
	v_cvt_pk_fp8_f32 v27, v38, v39 op_sel:[0,0,1]
	global_store_dwordx2 v[154:155], v[26:27], off
	s_cbranch_vccnz .LBB0_1081
	s_andn2_b64 vcc, exec, s[26:27]
	s_cbranch_vccnz .LBB0_1080
	s_barrier
	s_branch .LBB0_1080
